# baseline (speedup 1.0000x reference)
.LBB1_40:
	s_or_b64 exec, exec, s[4:5]
	v_lshrrev_b32_e32 v115, 5, v0
	v_mov_b32_e32 v4, s27
	v_mov_b32_e32 v5, s25
	v_cmp_eq_u32_e32 vcc, 3, v115
	v_lshrrev_b32_e32 v3, 5, v3
	s_movk_i32 s0, 0xa0
	v_cndmask_b32_e32 v99, v4, v5, vcc
	v_mov_b32_e32 v4, s26
	v_mov_b32_e32 v5, s24
	v_cndmask_b32_e32 v98, v4, v5, vcc
	v_lshlrev_b32_e32 v4, 2, v0
	v_lshlrev_b32_e32 v7, 4, v3
	v_lshlrev_b32_e32 v118, 2, v3
	v_mov_b32_e32 v3, 0
	s_lshl_b32 s33, s2, 6
	v_cmp_gt_u32_e64 s[2:3], s0, v0
	v_add_u32_e32 v116, 0x5200, v4
	s_movk_i32 s0, 0xdf
	v_add_u32_e32 v117, 0x5100, v4
	v_lshrrev_b32_e32 v5, 4, v0
	v_and_b32_e32 v4, 60, v4
	s_waitcnt lgkmcnt(0)
	v_lshl_add_u64 v[100:101], s[36:37], 0, v[2:3]
	v_mov_b32_e32 v2, 0x5200
	v_cmp_lt_u32_e64 s[6:7], s0, v0
	s_movk_i32 s0, 0x290
	v_lshl_or_b32 v119, v5, 2, v2
	v_lshlrev_b32_e32 v2, 2, v4
	v_lshlrev_b32_e32 v4, 1, v4
	v_mul_u32_u24_e32 v6, 0x290, v1
	v_mad_u32_u24 v120, v5, s0, v4
	v_or_b32_e32 v5, 16, v5
	v_cmp_lt_u32_e64 s[4:5], 31, v0
	v_lshl_add_u64 v[102:103], s[14:15], 0, v[2:3]
	v_mad_u32_u24 v121, v5, s0, v4
	v_lshl_add_u64 v[104:105], s[16:17], 0, v[2:3]
	v_lshl_add_u64 v[106:107], s[18:19], 0, v[2:3]
	v_lshl_add_u64 v[108:109], s[28:29], 0, v[2:3]
	v_lshl_add_u64 v[110:111], s[30:31], 0, v[2:3]
	v_or_b32_e32 v122, 0x5480, v7
	v_or_b32_e32 v123, 1, v118
	v_or_b32_e32 v124, 2, v118
	v_or_b32_e32 v125, 3, v118
	v_or_b32_e32 v126, 8, v118
	v_or_b32_e32 v127, 9, v118
	v_or_b32_e32 v128, 10, v118
	v_or_b32_e32 v129, 11, v118
	v_or_b32_e32 v130, 16, v118
	v_or_b32_e32 v131, 17, v118
	v_or_b32_e32 v132, 18, v118
	v_or_b32_e32 v133, 19, v118
	v_or_b32_e32 v134, 24, v118
	v_or_b32_e32 v135, 25, v118
	v_or_b32_e32 v136, 26, v118
	v_or_b32_e32 v137, 27, v118
	s_mov_b32 s16, 0
	s_mov_b32 s39, 1
	s_mov_b64 s[14:15], -1
	v_cmp_ne_u32_e64 s[8:9], 1, v115
	v_add_u32_e32 v138, v6, v7
	s_movk_i32 s28, 0x190
	s_movk_i32 s29, 0x64
	s_branch .LBB1_43

.LBB1_42:
	s_mov_b32 s16, 32
	s_mov_b32 s39, 0
	s_mov_b64 s[14:15], 0
	s_and_b64 vcc, exec, s[0:1]
	s_cbranch_vccnz .LBB1_63
.LBB1_43:
	s_or_b32 s30, s16, s33
	s_cmp_gt_i32 s30, 0x1869f
	s_mov_b64 s[0:1], -1
	s_cbranch_scc1 .LBB1_42
	s_cmp_eq_u32 s39, 0
	s_cbranch_scc1 .Lemb_skip_ld
	s_and_saveexec_b64 s[0:1], s[2:3]
	s_cbranch_execz .LBB1_52
	v_mov_b64_e32 v[2:3], s[20:21]
	s_and_saveexec_b64 s[16:17], s[4:5]
	s_cbranch_execz .LBB1_51
	v_cmp_lt_i32_e32 vcc, 1, v115
	s_mov_b64 s[18:19], 0
	s_and_saveexec_b64 s[24:25], vcc
	s_xor_b64 s[24:25], exec, s[24:25]
	s_cbranch_execnz .LBB1_59
	s_or_saveexec_b64 s[24:25], s[24:25]
	v_mov_b64_e32 v[2:3], s[34:35]
	s_xor_b64 exec, exec, s[24:25]
	s_cbranch_execnz .LBB1_62

.LBB1_51:
	s_or_b64 exec, exec, s[16:17]
	v_or_b32_e32 v4, s30, v1
	v_or_b32_e32 v6, 32, v4
	v_min_i32_e32 v4, 0x1869f, v4
	v_min_i32_e32 v6, 0x1869f, v6
	v_ashrrev_i32_e32 v5, 31, v4
	v_ashrrev_i32_e32 v7, 31, v6
	v_lshl_add_u64 v[8:9], v[6:7], 2, v[2:3]
	v_lshl_add_u64 v[2:3], v[4:5], 2, v[2:3]
	global_load_dword v2, v[2:3], off
	global_load_dword v8, v[8:9], off
	s_waitcnt vmcnt(0)
	ds_write_b32 v116, v2
	ds_write_b32 v116, v8 offset:768
.LBB1_52:
	s_or_b64 exec, exec, s[0:1]
	s_xor_b64 s[0:1], s[14:15], -1
	s_and_saveexec_b64 s[14:15], s[6:7]
	s_cbranch_execz .LBB1_54
	v_add_u32_e32 v2, s30, v0
	v_add_u32_e32 v4, 32, v2
	v_min_i32_e32 v2, 0x1877f, v2
	v_min_i32_e32 v4, 0x1877f, v4
	v_ashrrev_i32_e32 v3, 31, v2
	v_ashrrev_i32_e32 v5, 31, v4
	v_lshl_add_u64 v[4:5], v[4:5], 2, s[12:13]
	v_lshl_add_u64 v[2:3], v[2:3], 2, s[12:13]
	global_load_dword v2, v[2:3], off offset:-896
	global_load_dword v4, v[4:5], off offset:-896
	s_waitcnt vmcnt(0)
	ds_write_b32 v117, v2
	ds_write_b32 v117, v4 offset:768

.Lemb_skip_ld:
	s_xor_b64 s[0:1], s[14:15], -1
	v_add_u32_e32 v119, 0x300, v119
	v_add_u32_e32 v122, 0x300, v122
	s_branch .LBB1_54

	.amdhsa_kernel _Z12embed_kernelPKiS0_S0_S0_S0_PKfS2_S2_S2_S2_S2_S2_S2_PKDv8_DF16_PfiS2_S2_PS3_S0_S0_PiS8_S8_P15HIP_vector_typeIiLj2EES8_
		.amdhsa_group_segment_fixed_size 22528
		.amdhsa_private_segment_fixed_size 0
		.amdhsa_kernarg_size 208
		.amdhsa_user_sgpr_count 2
		.amdhsa_user_sgpr_dispatch_ptr 0
		.amdhsa_user_sgpr_queue_ptr 0
		.amdhsa_user_sgpr_kernarg_segment_ptr 1
		.amdhsa_user_sgpr_dispatch_id 0
		.amdhsa_user_sgpr_kernarg_preload_length 0
		.amdhsa_user_sgpr_kernarg_preload_offset 0
		.amdhsa_user_sgpr_private_segment_size 0
		.amdhsa_uses_dynamic_stack 0
		.amdhsa_enable_private_segment 0
		.amdhsa_system_sgpr_workgroup_id_x 1
		.amdhsa_system_sgpr_workgroup_id_y 0
		.amdhsa_system_sgpr_workgroup_id_z 0
		.amdhsa_system_sgpr_workgroup_info 0
		.amdhsa_system_vgpr_workitem_id 0
		.amdhsa_next_free_vgpr 166
		.amdhsa_next_free_sgpr 75
		.amdhsa_accum_offset 168
		.amdhsa_reserve_vcc 1
		.amdhsa_float_round_mode_32 0
		.amdhsa_float_round_mode_16_64 0
		.amdhsa_float_denorm_mode_32 3
		.amdhsa_float_denorm_mode_16_64 3
		.amdhsa_dx10_clamp 1
		.amdhsa_ieee_mode 1
		.amdhsa_fp16_overflow 0
		.amdhsa_tg_split 0
		.amdhsa_exception_fp_ieee_invalid_op 0
		.amdhsa_exception_fp_denorm_src 0
		.amdhsa_exception_fp_ieee_div_zero 0
		.amdhsa_exception_fp_ieee_overflow 0
		.amdhsa_exception_fp_ieee_underflow 0
		.amdhsa_exception_fp_ieee_inexact 0
		.amdhsa_exception_int_div_zero 0
	.end_amdhsa_kernel

.LBB2_22:
	s_mov_b64 s[20:21], exec
	v_cmp_lt_i32_e64 s[40:41], 0, v91
	v_cmp_lt_i32_e64 s[42:43], 1, v91
	v_cmp_lt_i32_e64 s[44:45], 2, v91
	v_cmp_lt_i32_e64 s[46:47], 3, v91
	v_cmp_lt_i32_e64 s[48:49], 4, v91
	v_cmp_lt_i32_e64 s[50:51], 5, v91
	v_cmp_lt_i32_e64 s[52:53], 6, v91
	v_cmp_lt_i32_e64 s[54:55], 7, v91
	s_and_b64 exec, s[20:21], s[40:41]
	v_mad_i64_i32 v[124:125], s[6:7], v6, s23, v[122:123]
	global_load_dwordx4 v[84:87], v[124:125], off
	global_load_dwordx4 v[80:83], v[124:125], off offset:64
	global_load_dwordx4 v[28:31], v[124:125], off offset:128
	global_load_dwordx4 v[24:27], v[124:125], off offset:192
	global_load_dwordx4 v[20:23], v[124:125], off offset:256
	global_load_dwordx4 v[10:13], v[124:125], off offset:320
	global_load_dwordx4 v[132:135], v[124:125], off offset:384
	s_and_b64 exec, s[20:21], s[42:43]
	v_mad_i64_i32 v[224:225], s[6:7], v7, s23, v[122:123]
	global_load_dwordx4 v[136:139], v[224:225], off
	global_load_dwordx4 v[140:143], v[224:225], off offset:64
	global_load_dwordx4 v[144:147], v[224:225], off offset:128
	global_load_dwordx4 v[148:151], v[224:225], off offset:192
	global_load_dwordx4 v[152:155], v[224:225], off offset:256
	global_load_dwordx4 v[156:159], v[224:225], off offset:320
	global_load_dwordx4 v[160:163], v[224:225], off offset:384
	s_and_b64 exec, s[20:21], s[44:45]
	v_mad_i64_i32 v[226:227], s[6:7], v8, s23, v[122:123]
	global_load_dwordx4 v[164:167], v[226:227], off
	global_load_dwordx4 v[168:171], v[226:227], off offset:64
	global_load_dwordx4 v[172:175], v[226:227], off offset:128
	global_load_dwordx4 v[180:183], v[226:227], off offset:192
	global_load_dwordx4 v[184:187], v[226:227], off offset:256
	global_load_dwordx4 v[188:191], v[226:227], off offset:320
	global_load_dwordx4 v[192:195], v[226:227], off offset:384
	s_and_b64 exec, s[20:21], s[46:47]
	v_mad_i64_i32 v[228:229], s[6:7], v9, s23, v[122:123]
	global_load_dwordx4 v[196:199], v[228:229], off
	global_load_dwordx4 v[200:203], v[228:229], off offset:64
	global_load_dwordx4 v[204:207], v[228:229], off offset:128
	global_load_dwordx4 v[208:211], v[228:229], off offset:192
	global_load_dwordx4 v[212:215], v[228:229], off offset:256
	global_load_dwordx4 v[216:219], v[228:229], off offset:320
	global_load_dwordx4 v[220:223], v[228:229], off offset:384
	s_and_b64 s[56:57], s[20:21], s[48:49]
	s_cmp_lg_u64 s[56:57], 0
	s_cbranch_scc1 .Lgru_long
	s_waitcnt vmcnt(0)
	s_and_b64 exec, s[20:21], s[40:41]
	v_pk_add_f32 v[108:109], v[84:85], v[108:109]
	v_pk_add_f32 v[118:119], v[86:87], v[118:119]
	v_pk_add_f32 v[116:117], v[80:81], v[116:117]
	v_pk_add_f32 v[114:115], v[82:83], v[114:115]
	v_pk_add_f32 v[112:113], v[28:29], v[112:113]
	v_pk_add_f32 v[110:111], v[30:31], v[110:111]
	v_pk_add_f32 v[106:107], v[24:25], v[106:107]
	v_pk_add_f32 v[104:105], v[26:27], v[104:105]
	v_pk_add_f32 v[102:103], v[20:21], v[102:103]
	v_pk_add_f32 v[100:101], v[22:23], v[100:101]
	v_pk_add_f32 v[98:99], v[10:11], v[98:99]
	v_pk_add_f32 v[96:97], v[12:13], v[96:97]
	s_and_b64 exec, exec, vcc
	v_pk_add_f32 v[94:95], v[132:133], v[94:95]
	v_pk_add_f32 v[92:93], v[134:135], v[92:93]
	s_and_b64 exec, s[20:21], s[42:43]
	v_pk_add_f32 v[108:109], v[136:137], v[108:109]
	v_pk_add_f32 v[118:119], v[138:139], v[118:119]
	v_pk_add_f32 v[116:117], v[140:141], v[116:117]
	v_pk_add_f32 v[114:115], v[142:143], v[114:115]
	v_pk_add_f32 v[112:113], v[144:145], v[112:113]
	v_pk_add_f32 v[110:111], v[146:147], v[110:111]
	v_pk_add_f32 v[106:107], v[148:149], v[106:107]
	v_pk_add_f32 v[104:105], v[150:151], v[104:105]
	v_pk_add_f32 v[102:103], v[152:153], v[102:103]
	v_pk_add_f32 v[100:101], v[154:155], v[100:101]
	v_pk_add_f32 v[98:99], v[156:157], v[98:99]
	v_pk_add_f32 v[96:97], v[158:159], v[96:97]
	s_and_b64 exec, exec, vcc
	v_pk_add_f32 v[94:95], v[160:161], v[94:95]
	v_pk_add_f32 v[92:93], v[162:163], v[92:93]
	s_and_b64 exec, s[20:21], s[44:45]
	v_pk_add_f32 v[108:109], v[164:165], v[108:109]
	v_pk_add_f32 v[118:119], v[166:167], v[118:119]
	v_pk_add_f32 v[116:117], v[168:169], v[116:117]
	v_pk_add_f32 v[114:115], v[170:171], v[114:115]
	v_pk_add_f32 v[112:113], v[172:173], v[112:113]
	v_pk_add_f32 v[110:111], v[174:175], v[110:111]
	v_pk_add_f32 v[106:107], v[180:181], v[106:107]
	v_pk_add_f32 v[104:105], v[182:183], v[104:105]
	v_pk_add_f32 v[102:103], v[184:185], v[102:103]
	v_pk_add_f32 v[100:101], v[186:187], v[100:101]
	v_pk_add_f32 v[98:99], v[188:189], v[98:99]
	v_pk_add_f32 v[96:97], v[190:191], v[96:97]
	s_and_b64 exec, exec, vcc
	v_pk_add_f32 v[94:95], v[192:193], v[94:95]
	v_pk_add_f32 v[92:93], v[194:195], v[92:93]
	s_and_b64 exec, s[20:21], s[46:47]
	v_pk_add_f32 v[108:109], v[196:197], v[108:109]
	v_pk_add_f32 v[118:119], v[198:199], v[118:119]
	v_pk_add_f32 v[116:117], v[200:201], v[116:117]
	v_pk_add_f32 v[114:115], v[202:203], v[114:115]
	v_pk_add_f32 v[112:113], v[204:205], v[112:113]
	v_pk_add_f32 v[110:111], v[206:207], v[110:111]
	v_pk_add_f32 v[106:107], v[208:209], v[106:107]
	v_pk_add_f32 v[104:105], v[210:211], v[104:105]
	v_pk_add_f32 v[102:103], v[212:213], v[102:103]
	v_pk_add_f32 v[100:101], v[214:215], v[100:101]
	v_pk_add_f32 v[98:99], v[216:217], v[98:99]
	v_pk_add_f32 v[96:97], v[218:219], v[96:97]
	s_and_b64 exec, exec, vcc
	v_pk_add_f32 v[94:95], v[220:221], v[94:95]
	v_pk_add_f32 v[92:93], v[222:223], v[92:93]
	s_branch .Lgru_gdone
.Lgru_long:
	s_waitcnt vmcnt(21)
	s_and_b64 exec, s[20:21], s[40:41]
	v_pk_add_f32 v[108:109], v[84:85], v[108:109]
	v_pk_add_f32 v[118:119], v[86:87], v[118:119]
	v_pk_add_f32 v[116:117], v[80:81], v[116:117]
	v_pk_add_f32 v[114:115], v[82:83], v[114:115]
	v_pk_add_f32 v[112:113], v[28:29], v[112:113]
	v_pk_add_f32 v[110:111], v[30:31], v[110:111]
	v_pk_add_f32 v[106:107], v[24:25], v[106:107]
	v_pk_add_f32 v[104:105], v[26:27], v[104:105]
	v_pk_add_f32 v[102:103], v[20:21], v[102:103]
	v_pk_add_f32 v[100:101], v[22:23], v[100:101]
	v_pk_add_f32 v[98:99], v[10:11], v[98:99]
	v_pk_add_f32 v[96:97], v[12:13], v[96:97]
	s_and_b64 exec, exec, vcc
	v_pk_add_f32 v[94:95], v[132:133], v[94:95]
	v_pk_add_f32 v[92:93], v[134:135], v[92:93]
	s_and_b64 exec, s[20:21], s[48:49]
	v_mad_i64_i32 v[124:125], s[6:7], v2, s23, v[122:123]
	global_load_dwordx4 v[84:87], v[124:125], off
	global_load_dwordx4 v[80:83], v[124:125], off offset:64
	global_load_dwordx4 v[28:31], v[124:125], off offset:128
	global_load_dwordx4 v[24:27], v[124:125], off offset:192
	global_load_dwordx4 v[20:23], v[124:125], off offset:256
	global_load_dwordx4 v[10:13], v[124:125], off offset:320
	global_load_dwordx4 v[132:135], v[124:125], off offset:384
	s_waitcnt vmcnt(21)
	s_and_b64 exec, s[20:21], s[42:43]
	v_pk_add_f32 v[108:109], v[136:137], v[108:109]
	v_pk_add_f32 v[118:119], v[138:139], v[118:119]
	v_pk_add_f32 v[116:117], v[140:141], v[116:117]
	v_pk_add_f32 v[114:115], v[142:143], v[114:115]
	v_pk_add_f32 v[112:113], v[144:145], v[112:113]
	v_pk_add_f32 v[110:111], v[146:147], v[110:111]
	v_pk_add_f32 v[106:107], v[148:149], v[106:107]
	v_pk_add_f32 v[104:105], v[150:151], v[104:105]
	v_pk_add_f32 v[102:103], v[152:153], v[102:103]
	v_pk_add_f32 v[100:101], v[154:155], v[100:101]
	v_pk_add_f32 v[98:99], v[156:157], v[98:99]
	v_pk_add_f32 v[96:97], v[158:159], v[96:97]
	s_and_b64 exec, exec, vcc
	v_pk_add_f32 v[94:95], v[160:161], v[94:95]
	v_pk_add_f32 v[92:93], v[162:163], v[92:93]
	s_and_b64 exec, s[20:21], s[50:51]
	v_mad_i64_i32 v[224:225], s[6:7], v3, s23, v[122:123]
	global_load_dwordx4 v[136:139], v[224:225], off
	global_load_dwordx4 v[140:143], v[224:225], off offset:64
	global_load_dwordx4 v[144:147], v[224:225], off offset:128
	global_load_dwordx4 v[148:151], v[224:225], off offset:192
	global_load_dwordx4 v[152:155], v[224:225], off offset:256
	global_load_dwordx4 v[156:159], v[224:225], off offset:320
	global_load_dwordx4 v[160:163], v[224:225], off offset:384
	s_waitcnt vmcnt(21)
	s_and_b64 exec, s[20:21], s[44:45]
	v_pk_add_f32 v[108:109], v[164:165], v[108:109]
	v_pk_add_f32 v[118:119], v[166:167], v[118:119]
	v_pk_add_f32 v[116:117], v[168:169], v[116:117]
	v_pk_add_f32 v[114:115], v[170:171], v[114:115]
	v_pk_add_f32 v[112:113], v[172:173], v[112:113]
	v_pk_add_f32 v[110:111], v[174:175], v[110:111]
	v_pk_add_f32 v[106:107], v[180:181], v[106:107]
	v_pk_add_f32 v[104:105], v[182:183], v[104:105]
	v_pk_add_f32 v[102:103], v[184:185], v[102:103]
	v_pk_add_f32 v[100:101], v[186:187], v[100:101]
	v_pk_add_f32 v[98:99], v[188:189], v[98:99]
	v_pk_add_f32 v[96:97], v[190:191], v[96:97]
	s_and_b64 exec, exec, vcc
	v_pk_add_f32 v[94:95], v[192:193], v[94:95]
	v_pk_add_f32 v[92:93], v[194:195], v[92:93]
	s_and_b64 exec, s[20:21], s[52:53]
	v_mad_i64_i32 v[226:227], s[6:7], v4, s23, v[122:123]
	global_load_dwordx4 v[164:167], v[226:227], off
	global_load_dwordx4 v[168:171], v[226:227], off offset:64
	global_load_dwordx4 v[172:175], v[226:227], off offset:128
	global_load_dwordx4 v[180:183], v[226:227], off offset:192
	global_load_dwordx4 v[184:187], v[226:227], off offset:256
	global_load_dwordx4 v[188:191], v[226:227], off offset:320
	global_load_dwordx4 v[192:195], v[226:227], off offset:384
	s_waitcnt vmcnt(21)
	s_and_b64 exec, s[20:21], s[46:47]
	v_pk_add_f32 v[108:109], v[196:197], v[108:109]
	v_pk_add_f32 v[118:119], v[198:199], v[118:119]
	v_pk_add_f32 v[116:117], v[200:201], v[116:117]
	v_pk_add_f32 v[114:115], v[202:203], v[114:115]
	v_pk_add_f32 v[112:113], v[204:205], v[112:113]
	v_pk_add_f32 v[110:111], v[206:207], v[110:111]
	v_pk_add_f32 v[106:107], v[208:209], v[106:107]
	v_pk_add_f32 v[104:105], v[210:211], v[104:105]
	v_pk_add_f32 v[102:103], v[212:213], v[102:103]
	v_pk_add_f32 v[100:101], v[214:215], v[100:101]
	v_pk_add_f32 v[98:99], v[216:217], v[98:99]
	v_pk_add_f32 v[96:97], v[218:219], v[96:97]
	s_and_b64 exec, exec, vcc
	v_pk_add_f32 v[94:95], v[220:221], v[94:95]
	v_pk_add_f32 v[92:93], v[222:223], v[92:93]
	s_and_b64 exec, s[20:21], s[54:55]
	v_mad_i64_i32 v[228:229], s[6:7], v5, s23, v[122:123]
	global_load_dwordx4 v[196:199], v[228:229], off
	global_load_dwordx4 v[200:203], v[228:229], off offset:64
	global_load_dwordx4 v[204:207], v[228:229], off offset:128
	global_load_dwordx4 v[208:211], v[228:229], off offset:192
	global_load_dwordx4 v[212:215], v[228:229], off offset:256
	global_load_dwordx4 v[216:219], v[228:229], off offset:320
	global_load_dwordx4 v[220:223], v[228:229], off offset:384
	s_waitcnt vmcnt(21)
	s_and_b64 exec, s[20:21], s[48:49]
	v_pk_add_f32 v[108:109], v[84:85], v[108:109]
	v_pk_add_f32 v[118:119], v[86:87], v[118:119]
	v_pk_add_f32 v[116:117], v[80:81], v[116:117]
	v_pk_add_f32 v[114:115], v[82:83], v[114:115]
	v_pk_add_f32 v[112:113], v[28:29], v[112:113]
	v_pk_add_f32 v[110:111], v[30:31], v[110:111]
	v_pk_add_f32 v[106:107], v[24:25], v[106:107]
	v_pk_add_f32 v[104:105], v[26:27], v[104:105]
	v_pk_add_f32 v[102:103], v[20:21], v[102:103]
	v_pk_add_f32 v[100:101], v[22:23], v[100:101]
	v_pk_add_f32 v[98:99], v[10:11], v[98:99]
	v_pk_add_f32 v[96:97], v[12:13], v[96:97]
	s_and_b64 exec, exec, vcc
	v_pk_add_f32 v[94:95], v[132:133], v[94:95]
	v_pk_add_f32 v[92:93], v[134:135], v[92:93]
	s_waitcnt vmcnt(14)
	s_and_b64 exec, s[20:21], s[50:51]
	v_pk_add_f32 v[108:109], v[136:137], v[108:109]
	v_pk_add_f32 v[118:119], v[138:139], v[118:119]
	v_pk_add_f32 v[116:117], v[140:141], v[116:117]
	v_pk_add_f32 v[114:115], v[142:143], v[114:115]
	v_pk_add_f32 v[112:113], v[144:145], v[112:113]
	v_pk_add_f32 v[110:111], v[146:147], v[110:111]
	v_pk_add_f32 v[106:107], v[148:149], v[106:107]
	v_pk_add_f32 v[104:105], v[150:151], v[104:105]
	v_pk_add_f32 v[102:103], v[152:153], v[102:103]
	v_pk_add_f32 v[100:101], v[154:155], v[100:101]
	v_pk_add_f32 v[98:99], v[156:157], v[98:99]
	v_pk_add_f32 v[96:97], v[158:159], v[96:97]
	s_and_b64 exec, exec, vcc
	v_pk_add_f32 v[94:95], v[160:161], v[94:95]
	v_pk_add_f32 v[92:93], v[162:163], v[92:93]
	s_waitcnt vmcnt(7)
	s_and_b64 exec, s[20:21], s[52:53]
	v_pk_add_f32 v[108:109], v[164:165], v[108:109]
	v_pk_add_f32 v[118:119], v[166:167], v[118:119]
	v_pk_add_f32 v[116:117], v[168:169], v[116:117]
	v_pk_add_f32 v[114:115], v[170:171], v[114:115]
	v_pk_add_f32 v[112:113], v[172:173], v[112:113]
	v_pk_add_f32 v[110:111], v[174:175], v[110:111]
	v_pk_add_f32 v[106:107], v[180:181], v[106:107]
	v_pk_add_f32 v[104:105], v[182:183], v[104:105]
	v_pk_add_f32 v[102:103], v[184:185], v[102:103]
	v_pk_add_f32 v[100:101], v[186:187], v[100:101]
	v_pk_add_f32 v[98:99], v[188:189], v[98:99]
	v_pk_add_f32 v[96:97], v[190:191], v[96:97]
	s_and_b64 exec, exec, vcc
	v_pk_add_f32 v[94:95], v[192:193], v[94:95]
	v_pk_add_f32 v[92:93], v[194:195], v[92:93]
	s_waitcnt vmcnt(0)
	s_and_b64 exec, s[20:21], s[54:55]
	v_pk_add_f32 v[108:109], v[196:197], v[108:109]
	v_pk_add_f32 v[118:119], v[198:199], v[118:119]
	v_pk_add_f32 v[116:117], v[200:201], v[116:117]
	v_pk_add_f32 v[114:115], v[202:203], v[114:115]
	v_pk_add_f32 v[112:113], v[204:205], v[112:113]
	v_pk_add_f32 v[110:111], v[206:207], v[110:111]
	v_pk_add_f32 v[106:107], v[208:209], v[106:107]
	v_pk_add_f32 v[104:105], v[210:211], v[104:105]
	v_pk_add_f32 v[102:103], v[212:213], v[102:103]
	v_pk_add_f32 v[100:101], v[214:215], v[100:101]
	v_pk_add_f32 v[98:99], v[216:217], v[98:99]
	v_pk_add_f32 v[96:97], v[218:219], v[96:97]
	s_and_b64 exec, exec, vcc
	v_pk_add_f32 v[94:95], v[220:221], v[94:95]
	v_pk_add_f32 v[92:93], v[222:223], v[92:93]
.Lgru_gdone:
	s_mov_b64 exec, s[20:21]
.LBB2_37:
	s_or_b64 exec, exec, s[18:19]

amdhsa.kernels:
  - .agpr_count:     0
    .args:
      - .actual_access:  read_only
        .address_space:  global
        .offset:         0
        .size:           8
        .value_kind:     global_buffer
      - .actual_access:  read_only
        .address_space:  global
        .offset:         8
        .size:           8
        .value_kind:     global_buffer
      - .actual_access:  read_only
        .address_space:  global
        .offset:         16
        .size:           8
        .value_kind:     global_buffer
      - .actual_access:  read_only
        .address_space:  global
        .offset:         24
        .size:           8
        .value_kind:     global_buffer
      - .actual_access:  read_only
        .address_space:  global
        .offset:         32
        .size:           8
        .value_kind:     global_buffer
      - .actual_access:  write_only
        .address_space:  global
        .offset:         40
        .size:           8
        .value_kind:     global_buffer
      - .actual_access:  write_only
        .address_space:  global
        .offset:         48
        .size:           8
        .value_kind:     global_buffer
      - .actual_access:  write_only
        .address_space:  global
        .offset:         56
        .size:           8
        .value_kind:     global_buffer
    .group_segment_fixed_size: 0
    .kernarg_segment_align: 8
    .kernarg_segment_size: 64
    .language:       OpenCL C
    .language_version:
      - 2
      - 0
    .max_flat_workgroup_size: 256
    .name:           _Z11prep_kernelPKfS0_S0_S0_S0_PDv8_DF16_S2_Pi
    .private_segment_fixed_size: 0
    .sgpr_count:     26
    .sgpr_spill_count: 0
    .symbol:         _Z11prep_kernelPKfS0_S0_S0_S0_PDv8_DF16_S2_Pi.kd
    .uniform_work_group_size: 1
    .uses_dynamic_stack: false
    .vgpr_count:     22
    .vgpr_spill_count: 0
    .wavefront_size: 64
  - .agpr_count:     0
    .args:
      - .actual_access:  read_only
        .address_space:  global
        .offset:         0
        .size:           8
        .value_kind:     global_buffer
      - .actual_access:  read_only
        .address_space:  global
        .offset:         8
        .size:           8
        .value_kind:     global_buffer
      - .actual_access:  read_only
        .address_space:  global
        .offset:         16
        .size:           8
        .value_kind:     global_buffer
      - .actual_access:  read_only
        .address_space:  global
        .offset:         24
        .size:           8
        .value_kind:     global_buffer
      - .actual_access:  read_only
        .address_space:  global
        .offset:         32
        .size:           8
        .value_kind:     global_buffer
      - .actual_access:  read_only
        .address_space:  global
        .offset:         40
        .size:           8
        .value_kind:     global_buffer
      - .actual_access:  read_only
        .address_space:  global
        .offset:         48
        .size:           8
        .value_kind:     global_buffer
      - .actual_access:  read_only
        .address_space:  global
        .offset:         56
        .size:           8
        .value_kind:     global_buffer
      - .actual_access:  read_only
        .address_space:  global
        .offset:         64
        .size:           8
        .value_kind:     global_buffer
      - .actual_access:  read_only
        .address_space:  global
        .offset:         72
        .size:           8
        .value_kind:     global_buffer
      - .actual_access:  read_only
        .address_space:  global
        .offset:         80
        .size:           8
        .value_kind:     global_buffer
      - .actual_access:  read_only
        .address_space:  global
        .offset:         88
        .size:           8
        .value_kind:     global_buffer
      - .actual_access:  read_only
        .address_space:  global
        .offset:         96
        .size:           8
        .value_kind:     global_buffer
      - .actual_access:  read_only
        .address_space:  global
        .offset:         104
        .size:           8
        .value_kind:     global_buffer
      - .actual_access:  write_only
        .address_space:  global
        .offset:         112
        .size:           8
        .value_kind:     global_buffer
      - .offset:         120
        .size:           4
        .value_kind:     by_value
      - .actual_access:  read_only
        .address_space:  global
        .offset:         128
        .size:           8
        .value_kind:     global_buffer
      - .actual_access:  read_only
        .address_space:  global
        .offset:         136
        .size:           8
        .value_kind:     global_buffer
      - .actual_access:  write_only
        .address_space:  global
        .offset:         144
        .size:           8
        .value_kind:     global_buffer
      - .actual_access:  read_only
        .address_space:  global
        .offset:         152
        .size:           8
        .value_kind:     global_buffer
      - .actual_access:  read_only
        .address_space:  global
        .offset:         160
        .size:           8
        .value_kind:     global_buffer
      - .address_space:  global
        .offset:         168
        .size:           8
        .value_kind:     global_buffer
      - .actual_access:  write_only
        .address_space:  global
        .offset:         176
        .size:           8
        .value_kind:     global_buffer
      - .address_space:  global
        .offset:         184
        .size:           8
        .value_kind:     global_buffer
      - .actual_access:  write_only
        .address_space:  global
        .offset:         192
        .size:           8
        .value_kind:     global_buffer
      - .actual_access:  write_only
        .address_space:  global
        .offset:         200
        .size:           8
        .value_kind:     global_buffer
    .group_segment_fixed_size: 22528
    .kernarg_segment_align: 8
    .kernarg_segment_size: 208
    .language:       OpenCL C
    .language_version:
      - 2
      - 0
    .max_flat_workgroup_size: 256
    .name:           _Z12embed_kernelPKiS0_S0_S0_S0_PKfS2_S2_S2_S2_S2_S2_S2_PKDv8_DF16_PfiS2_S2_PS3_S0_S0_PiS8_S8_P15HIP_vector_typeIiLj2EES8_
    .private_segment_fixed_size: 0
    .sgpr_count:     44
    .sgpr_spill_count: 0
    .symbol:         _Z12embed_kernelPKiS0_S0_S0_S0_PKfS2_S2_S2_S2_S2_S2_S2_PKDv8_DF16_PfiS2_S2_PS3_S0_S0_PiS8_S8_P15HIP_vector_typeIiLj2EES8_.kd
    .uniform_work_group_size: 1
    .uses_dynamic_stack: false
    .vgpr_count:     166
    .vgpr_spill_count: 0
    .wavefront_size: 64
  - .agpr_count:     0
    .args:
      - .actual_access:  read_only
        .address_space:  global
        .offset:         0
        .size:           8
        .value_kind:     global_buffer
      - .actual_access:  read_only
        .address_space:  global
        .offset:         8
        .size:           8
        .value_kind:     global_buffer
      - .actual_access:  read_only
        .address_space:  global
        .offset:         16
        .size:           8
        .value_kind:     global_buffer
      - .actual_access:  read_only
        .address_space:  global
        .offset:         24
        .size:           8
        .value_kind:     global_buffer
      - .actual_access:  read_only
        .address_space:  global
        .offset:         32
        .size:           8
        .value_kind:     global_buffer
      - .actual_access:  read_only
        .address_space:  global
        .offset:         40
        .size:           8
        .value_kind:     global_buffer
      - .actual_access:  read_only
        .address_space:  global
        .offset:         48
        .size:           8
        .value_kind:     global_buffer
      - .actual_access:  read_only
        .address_space:  global
        .offset:         56
        .size:           8
        .value_kind:     global_buffer
      - .actual_access:  write_only
        .address_space:  global
        .offset:         64
        .size:           8
        .value_kind:     global_buffer
      - .offset:         72
        .size:           4
        .value_kind:     by_value
    .group_segment_fixed_size: 30720
    .kernarg_segment_align: 8
    .kernarg_segment_size: 76
    .language:       OpenCL C
    .language_version:
      - 2
      - 0
    .max_flat_workgroup_size: 256
    .name:           _Z10gru_kernelPKfPKiS2_S2_PK15HIP_vector_typeIiLj2EEPKDv8_DF16_S0_S0_Pfi
    .private_segment_fixed_size: 0
    .sgpr_count:     31
    .sgpr_spill_count: 0
    .symbol:         _Z10gru_kernelPKfPKiS2_S2_PK15HIP_vector_typeIiLj2EEPKDv8_DF16_S0_S0_Pfi.kd
    .uniform_work_group_size: 1
    .uses_dynamic_stack: false
    .vgpr_count:     231
    .vgpr_spill_count: 0
    .wavefront_size: 64
  - .agpr_count:     0
    .args:
      - .actual_access:  read_only
        .address_space:  global
        .offset:         0
        .size:           8
        .value_kind:     global_buffer
      - .actual_access:  read_only
        .address_space:  global
        .offset:         8
        .size:           8
        .value_kind:     global_buffer
      - .actual_access:  write_only
        .address_space:  global
        .offset:         16
        .size:           8
        .value_kind:     global_buffer
    .group_segment_fixed_size: 1024
    .kernarg_segment_align: 8
    .kernarg_segment_size: 24
    .language:       OpenCL C
    .language_version:
      - 2
      - 0
    .max_flat_workgroup_size: 256
    .name:           _Z11pool_kernelPKfPKiPDF16_
    .private_segment_fixed_size: 0
    .sgpr_count:     26
    .sgpr_spill_count: 0
    .symbol:         _Z11pool_kernelPKfPKiPDF16_.kd
    .uniform_work_group_size: 1
    .uses_dynamic_stack: false
    .vgpr_count:     31
    .vgpr_spill_count: 0
    .wavefront_size: 64
  - .agpr_count:     0
    .args:
      - .actual_access:  read_only
        .address_space:  global
        .offset:         0
        .size:           8
        .value_kind:     global_buffer
      - .actual_access:  read_only
        .address_space:  global
        .offset:         8
        .size:           8
        .value_kind:     global_buffer
      - .actual_access:  write_only
        .address_space:  global
        .offset:         16
        .size:           8
        .value_kind:     global_buffer
    .group_segment_fixed_size: 147456
    .kernarg_segment_align: 8
    .kernarg_segment_size: 24
    .language:       OpenCL C
    .language_version:
      - 2
      - 0
    .max_flat_workgroup_size: 256
    .name:           _Z9fc_kernelPKDv8_DF16_S1_Pf
    .private_segment_fixed_size: 0
    .sgpr_count:     17
    .sgpr_spill_count: 0
    .symbol:         _Z9fc_kernelPKDv8_DF16_S1_Pf.kd
    .uniform_work_group_size: 1
    .uses_dynamic_stack: false
    .vgpr_count:     208
    .vgpr_spill_count: 0
    .wavefront_size: 64
